# speedup vs baseline: 1.0571x; 1.0571x over previous
_Z5k_aggPKDF16_PKhPKiS4_PKDv8_DF16_PKfPDF16_Pf:
	s_load_dwordx8 s[4:11], s[0:1], 0x8
	s_load_dwordx4 s[12:15], s[0:1], 0x28
	s_load_dwordx2 s[16:17], s[0:1], 0x38
	v_lshlrev_b32_e32 v2, 4, v0
	s_lshl_b32 s0, s2, 2
	s_lshl_b32 s1, s2, 3
	s_andn2_b32 s0, s0, 63
	s_and_b32 s1, s1, 56
	s_or_b32 s0, s0, s1
	s_lshr_b32 s1, s2, 1
	s_and_b32 s1, s1, 4
	s_or_b32 s0, s0, s1
	v_lshlrev_b32_e32 v1, 2, v0
	v_lshrrev_b32_e32 v52, 6, v0
	v_or_b32_e32 v3, s0, v52
	v_mov_b32_e32 v98, v2
	s_waitcnt lgkmcnt(0)
	global_load_dwordx4 v[64:67], v2, s[10:11]
	v_add_u32_e32 v96, 0x1000, v2
	global_load_dwordx4 v[68:71], v96, s[10:11]
	v_add_u32_e32 v96, 0x2000, v2
	global_load_dwordx4 v[72:75], v96, s[10:11]
	v_add_u32_e32 v96, 0x3000, v2
	global_load_dwordx4 v[76:79], v96, s[10:11]
	v_add_u32_e32 v96, 0x4000, v2
	global_load_dwordx4 v[80:83], v96, s[10:11]
	v_add_u32_e32 v96, 0x5000, v2
	global_load_dwordx4 v[84:87], v96, s[10:11]
	v_add_u32_e32 v96, 0x6000, v2
	global_load_dwordx4 v[88:91], v96, s[10:11]
	v_add_u32_e32 v96, 0x7000, v2
	global_load_dwordx4 v[92:95], v96, s[10:11]
	v_mov_b32_e32 v97, 0
	ds_write2st64_b32 v1, v97, v97 offset0:128 offset1:132
	ds_write2st64_b32 v1, v97, v97 offset0:136 offset1:140
	s_movk_i32 s0, 0x186a
	v_cmp_gt_i32_e32 vcc, s0, v3
	s_and_saveexec_b64 s[0:1], vcc
	s_cbranch_execz .Lagg_invalid
	v_bfe_u32 v4, v0, 2, 4
	v_lshlrev_b32_e32 v53, 4, v3
	v_or_b32_e32 v10, v53, v4
	v_and_b32_e32 v54, 48, v2
	v_lshl_or_b32 v11, v10, 7, v54
	global_load_dwordx4 v[2:5], v11, s[4:5]
	global_load_dwordx4 v[6:9], v11, s[4:5] offset:64
	v_ashrrev_i32_e32 v11, 31, v10
	v_lshl_add_u64 v[10:11], v[10:11], 2, s[6:7]
	global_load_dwordx2 v[50:51], v[10:11], off
	s_waitcnt vmcnt(3)
	ds_write_b128 v98, v[64:67]
	ds_write_b128 v98, v[68:71] offset:4096
	ds_write_b128 v98, v[72:75] offset:8192
	ds_write_b128 v98, v[76:79] offset:12288
	ds_write_b128 v98, v[80:83] offset:16384
	ds_write_b128 v98, v[84:87] offset:20480
	ds_write_b128 v98, v[88:91] offset:24576
	ds_write_b128 v98, v[92:95] offset:28672
	s_waitcnt vmcnt(2)
	v_cvt_pk_f32_fp8_e32 v[10:11], v2
	v_cvt_pk_f32_fp8_sdwa v[12:13], v2 src0_sel:WORD_1
	v_cvt_pk_f32_fp8_e32 v[14:15], v3
	v_cvt_pk_f32_fp8_sdwa v[2:3], v3 src0_sel:WORD_1
	v_cvt_pk_f32_fp8_e32 v[16:17], v4
	v_cvt_pk_f32_fp8_sdwa v[18:19], v4 src0_sel:WORD_1
	v_cvt_pk_f32_fp8_e32 v[20:21], v5
	v_cvt_pk_f32_fp8_sdwa v[4:5], v5 src0_sel:WORD_1
	s_waitcnt vmcnt(1)
	v_cvt_pk_f32_fp8_e32 v[22:23], v6
	v_cvt_pk_f32_fp8_sdwa v[24:25], v6 src0_sel:WORD_1
	v_cvt_pk_f32_fp8_e32 v[26:27], v7
	v_cvt_pk_f32_fp8_sdwa v[6:7], v7 src0_sel:WORD_1
	v_cvt_pk_f32_fp8_e32 v[28:29], v8
	v_cvt_pk_f32_fp8_sdwa v[30:31], v8 src0_sel:WORD_1
	v_cvt_pk_f32_fp8_e32 v[32:33], v9
	v_cvt_pk_f32_fp8_sdwa v[8:9], v9 src0_sel:WORD_1
	v_add_f32_e32 v88, 0, v10
	v_add_f32_e32 v89, 0, v11
	v_add_f32_e32 v90, 0, v12
	v_add_f32_e32 v91, 0, v13
	v_add_f32_e32 v92, 0, v14
	v_add_f32_e32 v93, 0, v15
	v_add_f32_e32 v94, 0, v2
	v_add_f32_e32 v95, 0, v3
	v_add_f32_e32 v76, 0, v16
	v_add_f32_e32 v77, 0, v17
	v_add_f32_e32 v80, 0, v18
	v_add_f32_e32 v81, 0, v19
	v_add_f32_e32 v84, 0, v20
	v_add_f32_e32 v85, 0, v21
	v_add_f32_e32 v86, 0, v4
	v_add_f32_e32 v87, 0, v5
	v_add_f32_e32 v72, 0, v22
	v_add_f32_e32 v73, 0, v23
	v_add_f32_e32 v74, 0, v24
	v_add_f32_e32 v75, 0, v25
	v_add_f32_e32 v78, 0, v26
	v_add_f32_e32 v79, 0, v27
	v_add_f32_e32 v82, 0, v6
	v_add_f32_e32 v83, 0, v7
	v_add_f32_e32 v64, 0, v28
	v_add_f32_e32 v65, 0, v29
	v_add_f32_e32 v66, 0, v30
	v_add_f32_e32 v67, 0, v31
	v_add_f32_e32 v68, 0, v32
	v_add_f32_e32 v69, 0, v33
	v_add_f32_e32 v70, 0, v8
	v_add_f32_e32 v71, 0, v9
	s_waitcnt vmcnt(0)
	v_cmp_lt_i32_e32 vcc, v50, v51
	s_and_saveexec_b64 s[6:7], vcc
	s_cbranch_execz .LBB2_7
	v_add_u32_e32 v55, -1, v51
	v_min_i32_e32 v2, v50, v55
	v_max_i32_e32 v2, 0, v2
	v_mov_b32_e32 v3, 0
	v_lshl_add_u64 v[4:5], v[2:3], 2, s[8:9]
	v_add_u32_e32 v2, 1, v50
	v_min_i32_e32 v2, v2, v55
	v_max_i32_e32 v2, 0, v2
	v_lshl_add_u64 v[6:7], v[2:3], 2, s[8:9]
	v_add_u32_e32 v2, 2, v50
	v_min_i32_e32 v2, v2, v55
	v_max_i32_e32 v2, 0, v2
	v_lshl_add_u64 v[8:9], v[2:3], 2, s[8:9]
	v_add_u32_e32 v2, 3, v50
	v_min_i32_e32 v2, v2, v55
	v_max_i32_e32 v2, 0, v2
	v_lshl_add_u64 v[10:11], v[2:3], 2, s[8:9]
	v_add_u32_e32 v2, 4, v50
	v_min_i32_e32 v2, v2, v55
	v_max_i32_e32 v2, 0, v2
	v_lshl_add_u64 v[12:13], v[2:3], 2, s[8:9]
	v_add_u32_e32 v2, 5, v50
	v_min_i32_e32 v2, v2, v55
	v_max_i32_e32 v2, 0, v2
	v_lshl_add_u64 v[2:3], v[2:3], 2, s[8:9]
	global_load_dword v57, v[4:5], off
	global_load_dword v60, v[6:7], off
	global_load_dword v58, v[8:9], off
	global_load_dword v59, v[10:11], off
	global_load_dword v61, v[12:13], off
	global_load_dword v62, v[2:3], off
	v_add_u32_e32 v50, 11, v50
	s_mov_b64 s[10:11], 0
	v_mov_b32_e32 v56, 0xc35000

.LBB2_7:
	s_or_b64 exec, exec, s[6:7]
	s_waitcnt lgkmcnt(0)
	s_barrier
	v_and_b32_e32 v2, 63, v0
	v_lshrrev_b32_e32 v100, 4, v2
	v_and_or_b32 v3, v1, 60, v100
	v_lshlrev_b32_e32 v101, 2, v3
	v_cvt_pk_f16_f32 v3, v94, v95
	v_cvt_pk_f16_f32 v6, v92, v93
	v_cvt_pk_f16_f32 v5, v90, v91
	v_cvt_pk_f16_f32 v4, v88, v89
	ds_bpermute_b32 v4, v101, v4
	ds_bpermute_b32 v5, v101, v5
	ds_bpermute_b32 v6, v101, v6
	ds_bpermute_b32 v7, v101, v3
	v_lshlrev_b32_e32 v102, 4, v2
	v_cvt_pk_f16_f32 v2, v86, v87
	v_cvt_pk_f16_f32 v3, v84, v85
	s_waitcnt vmcnt(0)
	v_cvt_pk_f16_f32 v62, v80, v81
	v_cvt_pk_f16_f32 v63, v76, v77
	ds_bpermute_b32 v84, v101, v63
	ds_bpermute_b32 v85, v101, v62
	ds_bpermute_b32 v86, v101, v3
	ds_bpermute_b32 v87, v101, v2
	ds_read_b128 v[8:11], v102
	ds_read_b128 v[12:15], v102 offset:1024
	ds_read_b128 v[16:19], v102 offset:4096
	ds_read_b128 v[20:23], v102 offset:8192
	ds_read_b128 v[24:27], v102 offset:5120
	ds_read_b128 v[28:31], v102 offset:12288
	ds_read_b128 v[32:35], v102 offset:9216
	ds_read_b128 v[36:39], v102 offset:16384
	ds_read_b128 v[40:43], v102 offset:13312
	ds_read_b128 v[44:47], v102 offset:20480
	ds_read_b128 v[48:51], v102 offset:17408
	ds_read_b128 v[54:57], v102 offset:24576
	ds_read_b128 v[58:61], v102 offset:21504
	ds_read_b128 v[88:91], v102 offset:28672
	ds_read_b128 v[92:95], v102 offset:25600
	s_waitcnt lgkmcnt(14)
	v_mfma_f32_16x16x32_f16 v[8:11], v[4:7], v[8:11], 0
	v_lshlrev_b32_e32 v2, 3, v0
	v_and_b32_e32 v103, 0x78, v2
	v_lshlrev_b32_e32 v104, 2, v103
	s_waitcnt lgkmcnt(12)
	v_mfma_f32_16x16x32_f16 v[16:19], v[4:7], v[16:19], 0
	v_cvt_pk_f16_f32 v2, v82, v83
	v_cvt_pk_f16_f32 v3, v78, v79
	ds_read_b128 v[96:99], v102 offset:29696
	s_waitcnt lgkmcnt(12)
	v_mfma_f32_16x16x32_f16 v[20:23], v[4:7], v[20:23], 0
	v_cvt_pk_f16_f32 v66, v66, v67
	v_cvt_pk_f16_f32 v67, v64, v65
	s_waitcnt lgkmcnt(10)
	v_mfma_f32_16x16x32_f16 v[28:31], v[4:7], v[28:31], 0
	s_waitcnt lgkmcnt(8)
	v_mfma_f32_16x16x32_f16 v[36:39], v[4:7], v[36:39], 0
	s_waitcnt lgkmcnt(6)
	v_mfma_f32_16x16x32_f16 v[44:47], v[4:7], v[44:47], 0
	s_waitcnt lgkmcnt(4)
	v_mfma_f32_16x16x32_f16 v[54:57], v[4:7], v[54:57], 0
	s_waitcnt lgkmcnt(2)
	v_mfma_f32_16x16x32_f16 v[88:91], v[4:7], v[88:91], 0
	v_cvt_pk_f16_f32 v4, v74, v75
	v_cvt_pk_f16_f32 v5, v72, v73
	v_mfma_f32_16x16x32_f16 v[10:13], v[84:87], v[12:15], v[8:11]
	v_mfma_f32_16x16x32_f16 v[14:17], v[84:87], v[24:27], v[16:19]
	s_nop 1
	global_load_dwordx4 v[6:9], v104, s[12:13] offset:16
	v_mfma_f32_16x16x32_f16 v[18:21], v[84:87], v[32:35], v[20:23]
	ds_bpermute_b32 v32, v101, v3
	ds_bpermute_b32 v33, v101, v2
	v_mfma_f32_16x16x32_f16 v[22:25], v[84:87], v[40:43], v[28:31]
	s_nop 2
	ds_bpermute_b32 v30, v101, v5
	ds_bpermute_b32 v31, v101, v4
	global_load_dwordx4 v[2:5], v104, s[12:13]
	v_mfma_f32_16x16x32_f16 v[26:29], v[84:87], v[48:51], v[36:39]
	v_cvt_pk_f16_f32 v50, v70, v71
	v_cvt_pk_f16_f32 v51, v68, v69
	v_mfma_f32_16x16x32_f16 v[34:37], v[84:87], v[58:61], v[44:47]
	s_nop 2
	ds_read_b128 v[46:49], v102 offset:2048
	s_waitcnt lgkmcnt(6)
	v_mfma_f32_16x16x32_f16 v[38:41], v[84:87], v[92:95], v[54:57]
	s_nop 2
	ds_read_b128 v[54:57], v102 offset:3072
	s_waitcnt lgkmcnt(1)
	v_mfma_f32_16x16x32_f16 v[10:13], v[30:33], v[46:49], v[10:13]
	ds_read_b128 v[46:49], v102 offset:6144
	ds_read_b128 v[58:61], v102 offset:10240
	ds_read_b128 v[72:75], v102 offset:7168
	s_waitcnt lgkmcnt(2)
	v_mfma_f32_16x16x32_f16 v[14:17], v[30:33], v[46:49], v[14:17]
	ds_read_b128 v[46:49], v102 offset:14336
	ds_read_b128 v[76:79], v102 offset:11264
	s_waitcnt lgkmcnt(3)
	v_mfma_f32_16x16x32_f16 v[18:21], v[30:33], v[58:61], v[18:21]
	ds_read_b128 v[58:61], v102 offset:18432
	ds_read_b128 v[68:71], v102 offset:15360
	s_waitcnt lgkmcnt(3)
	v_mfma_f32_16x16x32_f16 v[22:25], v[30:33], v[46:49], v[22:25]
	ds_read_b128 v[46:49], v102 offset:22528
	ds_read_b128 v[80:83], v102 offset:19456
	s_waitcnt lgkmcnt(1)
	v_mfma_f32_16x16x32_f16 v[34:37], v[30:33], v[46:49], v[34:37]
	ds_bpermute_b32 v46, v101, v67
	ds_bpermute_b32 v47, v101, v66
	ds_bpermute_b32 v48, v101, v51
	ds_bpermute_b32 v49, v101, v50
	v_mfma_f32_16x16x32_f16 v[26:29], v[30:33], v[58:61], v[26:29]
	ds_read_b128 v[58:61], v102 offset:26624
	ds_read_b128 v[62:65], v102 offset:23552
	v_mfma_f32_16x16x32_f16 v[42:45], v[84:87], v[96:99], v[88:91]
	ds_read_b128 v[84:87], v102 offset:30720
	s_nop 1
	ds_read_b128 v[88:91], v102 offset:27648
	s_waitcnt lgkmcnt(3)
	v_mfma_f32_16x16x32_f16 v[38:41], v[30:33], v[58:61], v[38:41]
	ds_read_b128 v[58:61], v102 offset:31744
	s_waitcnt lgkmcnt(2)
	v_mfma_f32_16x16x32_f16 v[30:33], v[30:33], v[84:87], v[42:45]
	v_lshlrev_b32_e32 v85, 2, v100
	v_lshlrev_b32_e32 v84, 10, v52
	v_or_b32_e32 v66, v53, v85
	v_lshlrev_b32_e32 v42, 1, v103
	v_mov_b32_e32 v43, 0
	v_mfma_f32_16x16x32_f16 v[14:17], v[46:49], v[72:75], v[14:17]
	v_lshl_add_u64 v[72:73], s[14:15], 0, v[42:43]
	v_ashrrev_i32_e32 v67, 31, v66
	v_mfma_f32_16x16x32_f16 v[42:45], v[46:49], v[76:79], v[18:21]
	v_mfma_f32_16x16x32_f16 v[50:53], v[46:49], v[68:71], v[22:25]
	s_nop 3
	v_mov_b32_e32 v21, v14
	v_lshlrev_b64 v[18:19], 8, v[66:67]
	v_lshl_add_u64 v[74:75], v[72:73], 0, v[18:19]
	v_mfma_f32_16x16x32_f16 v[10:13], v[46:49], v[54:57], v[10:13]
	v_mov_b32_e32 v22, v42
	v_mov_b32_e32 v23, v50
	v_mov_b32_e32 v42, v15
	v_mfma_f32_16x16x32_f16 v[54:57], v[46:49], v[80:83], v[26:29]
	v_or_b32_e32 v18, 1, v66
	s_nop 2
	v_mov_b32_e32 v20, v10
	v_ashrrev_i32_e32 v19, 31, v18
	v_mfma_f32_16x16x32_f16 v[34:37], v[46:49], v[62:65], v[34:37]
	v_lshlrev_b64 v[18:19], 8, v[18:19]
	v_lshl_add_u64 v[68:69], v[72:73], 0, v[18:19]
	v_or_b32_e32 v18, 2, v66
	s_waitcnt lgkmcnt(1)
	v_mfma_f32_16x16x32_f16 v[38:41], v[46:49], v[88:91], v[38:41]
	s_waitcnt vmcnt(0)
	v_pk_add_f32 v[24:25], v[4:5], v[22:23]
	v_mov_b32_e32 v22, v54
	v_mov_b32_e32 v23, v34
	s_waitcnt lgkmcnt(0)
	v_mfma_f32_16x16x32_f16 v[28:31], v[46:49], v[58:61], v[30:33]
	v_add_f32_e64 v26, v6, v22
	v_add_f32_e64 v27, v7, v23
	v_mov_b32_e32 v22, v38
	v_pk_add_f32 v[20:21], v[2:3], v[20:21]
	v_add_f32_e32 v50, v2, v11
	v_cvt_pk_f16_f32 v46, v20, v21
	s_nop 1
	v_mov_b32_e32 v23, v28
	v_pk_add_f32 v[22:23], v[8:9], v[22:23]
	v_cvt_pk_f16_f32 v47, v24, v25
	v_cvt_pk_f16_f32 v48, v26, v27
	v_cvt_pk_f16_f32 v49, v22, v23
	v_cvt_f16_f32_e32 v14, v50
	global_store_dwordx4 v[74:75], v[46:49], off
	v_mov_b32_e32 v54, v51
	v_add_f32_e32 v51, v9, v29
	v_pk_mov_b32 v[46:47], v[2:3], v[4:5] op_sel:[1,0]
	v_pk_mov_b32 v[48:49], v[6:7], v[8:9] op_sel:[1,0]
	v_pk_add_f32 v[10:11], v[46:47], v[42:43]
	v_mov_b32_e32 v38, v35
	v_cvt_pk_f16_f32 v3, v10, v11
	v_pack_b32_f16 v32, v14, v3
	v_pk_mov_b32 v[14:15], v[4:5], v[6:7] op_sel:[1,0]
	v_pk_add_f32 v[28:29], v[48:49], v[38:39]
	v_pk_add_f32 v[42:43], v[14:15], v[54:55]
	v_cvt_pk_f16_f32 v5, v28, v29
	v_cvt_pk_f16_f32 v4, v42, v43
	v_alignbit_b32 v33, v4, v3, 16
	v_cvt_f16_f32_e32 v3, v51
	v_alignbit_b32 v34, v5, v4, 16
	v_add_f32_e32 v54, v2, v12
	v_mov_b32_e32 v6, v52
	v_alignbit_b32 v35, v3, v5, 16
	v_mov_b32_e32 v7, v56
	global_store_dwordx4 v[68:69], v[32:35], off
	v_cvt_f16_f32_e32 v3, v54
	v_mov_b32_e32 v4, v16
	v_pk_add_f32 v[34:35], v[14:15], v[6:7]
	v_mov_b32_e32 v6, v36
	v_add_f32_e32 v36, v9, v30
	v_mov_b32_e32 v5, v44
	v_cvt_f16_f32_e32 v8, v36
	v_add_f32_e32 v52, v2, v13
	v_pk_add_f32 v[32:33], v[46:47], v[4:5]
	v_mov_b32_e32 v7, v40
	v_cvt_f16_f32_e32 v2, v52
	v_ashrrev_i32_e32 v19, 31, v18
	v_cvt_pk_f16_f32 v5, v32, v33
	v_pk_add_f32 v[38:39], v[48:49], v[6:7]
	v_mov_b32_e32 v44, v17
	v_lshlrev_b64 v[18:19], 8, v[18:19]
	v_pack_b32_f16 v4, v3, v5
	v_cvt_pk_f16_f32 v3, v34, v35
	v_cvt_pk_f16_f32 v7, v38, v39
	v_pk_add_f32 v[12:13], v[46:47], v[44:45]
	v_mov_b32_e32 v56, v53
	v_mov_b32_e32 v40, v37
	v_lshl_add_u64 v[62:63], v[72:73], 0, v[18:19]
	v_alignbit_b32 v5, v3, v5, 16
	v_alignbit_b32 v6, v7, v3, 16
	v_alignbit_b32 v7, v8, v7, 16
	v_cvt_pk_f16_f32 v3, v12, v13
	v_pk_add_f32 v[14:15], v[14:15], v[56:57]
	v_pk_add_f32 v[16:17], v[48:49], v[40:41]
	global_store_dwordx4 v[62:63], v[4:7], off
	v_cvt_pk_f16_f32 v37, v16, v17
	v_add_f32_e32 v9, v9, v31
	v_pack_b32_f16 v6, v2, v3
	v_cvt_pk_f16_f32 v2, v14, v15
	v_alignbit_b32 v7, v2, v3, 16
	v_alignbit_b32 v8, v37, v2, 16
	v_pk_mul_f32 v[2:3], v[22:23], v[22:23]
	v_or_b32_e32 v18, 3, v66
	v_mul_f32_e32 v2, v29, v29
	v_pk_fma_f32 v[4:5], v[22:23], v[22:23], v[2:3] op_sel_hi:[1,1,0]
	v_mul_f32_e32 v2, v39, v39
	v_pk_add_f32 v[4:5], v[2:3], v[4:5] op_sel_hi:[0,1]
	v_mul_f32_e32 v2, v17, v17
	v_pk_add_f32 v[4:5], v[2:3], v[4:5] op_sel_hi:[0,1]
	v_add_f32_e32 v2, 0, v22
	v_add_f32_e32 v2, v29, v2
	v_add_f32_e32 v2, v39, v2
	v_add_f32_e32 v5, v17, v2
	v_mul_f32_e32 v2, v27, v27
	v_pk_fma_f32 v[30:31], v[28:29], v[28:29], v[2:3] op_sel_hi:[1,1,0]
	v_add_f32_e32 v2, 0, v27
	v_add_f32_e32 v2, v28, v2
	v_add_f32_e32 v2, v38, v2
	v_pk_fma_f32 v[30:31], v[38:39], v[38:39], v[30:31]
	v_add_f32_e32 v22, v16, v2
	v_mul_f32_e32 v2, v43, v43
	v_pk_fma_f32 v[30:31], v[16:17], v[16:17], v[30:31]
	v_pk_fma_f32 v[16:17], v[26:27], v[26:27], v[2:3] op_sel_hi:[1,1,0]
	v_mul_f32_e32 v2, v35, v35
	v_pk_add_f32 v[16:17], v[2:3], v[16:17] op_sel_hi:[0,1]
	v_mul_f32_e32 v2, v15, v15
	v_pk_add_f32 v[16:17], v[2:3], v[16:17] op_sel_hi:[0,1]
	v_add_f32_e32 v2, 0, v26
	v_add_f32_e32 v2, v43, v2
	v_add_f32_e32 v2, v35, v2
	v_add_f32_e32 v17, v15, v2
	v_mul_f32_e32 v2, v25, v25
	v_pk_fma_f32 v[26:27], v[42:43], v[42:43], v[2:3] op_sel_hi:[1,1,0]
	v_add_f32_e32 v2, 0, v25
	v_pk_fma_f32 v[26:27], v[34:35], v[34:35], v[26:27]
	v_add_f32_e32 v2, v42, v2
	v_pk_fma_f32 v[26:27], v[14:15], v[14:15], v[26:27]
	v_add_f32_e32 v2, v34, v2
	v_add_f32_e32 v27, v14, v2
	v_mul_f32_e32 v2, v11, v11
	v_pk_fma_f32 v[14:15], v[24:25], v[24:25], v[2:3] op_sel_hi:[1,1,0]
	v_mul_f32_e32 v2, v33, v33
	v_pk_add_f32 v[14:15], v[2:3], v[14:15] op_sel_hi:[0,1]
	v_mul_f32_e32 v2, v13, v13
	v_pk_add_f32 v[14:15], v[2:3], v[14:15] op_sel_hi:[0,1]
	v_add_f32_e32 v2, 0, v24
	v_pk_mul_f32 v[24:25], v[20:21], v[20:21]
	v_add_f32_e32 v2, v11, v2
	v_pk_fma_f32 v[28:29], v[10:11], v[10:11], v[24:25] op_sel:[0,0,1] op_sel_hi:[1,1,0]
	v_add_f32_e32 v11, 0, v21
	v_add_f32_e32 v2, v33, v2
	v_pk_fma_f32 v[28:29], v[32:33], v[32:33], v[28:29]
	v_add_f32_e32 v10, v10, v11
	v_add_f32_e32 v2, v13, v2
	v_pk_fma_f32 v[28:29], v[12:13], v[12:13], v[28:29]
	v_add_f32_e32 v10, v32, v10
	v_add_f32_e32 v11, 0, v20
	v_cvt_f16_f32_e32 v13, v9
	v_add_f32_e32 v10, v12, v10
	v_add_f32_e32 v11, v50, v11
	v_add_f32_e32 v12, 0, v23
	v_ashrrev_i32_e32 v19, 31, v18
	v_add_f32_e32 v11, v54, v11
	v_fmac_f32_e32 v3, v51, v51
	v_add_f32_e32 v12, v51, v12
	v_lshlrev_b64 v[18:19], 8, v[18:19]
	v_add_f32_e32 v11, v52, v11
	v_fmac_f32_e32 v3, v36, v36
	v_add_f32_e32 v12, v36, v12
	v_lshl_add_u64 v[18:19], v[72:73], 0, v[18:19]
	v_add_f32_e32 v12, v9, v12
	v_fmac_f32_e32 v3, v9, v9
	v_alignbit_b32 v9, v13, v37, 16
	v_permlane16_swap_b32_e32 v11, v10
	v_permlane16_swap_b32_e32 v2, v27
	global_store_dwordx4 v[18:19], v[6:9], off
	v_add_f32_e32 v2, v2, v27
	v_fmac_f32_e32 v24, v50, v50
	v_add_f32_e32 v6, v11, v10
	s_nop 1
	v_permlane32_swap_b32_e32 v6, v2
	v_permlane16_swap_b32_e32 v17, v22
	v_permlane16_swap_b32_e32 v5, v12
	v_fmac_f32_e32 v24, v54, v54
	v_add_f32_e32 v2, v6, v2
	v_add_f32_e32 v6, v17, v22
	v_add_f32_e32 v5, v5, v12
	v_or3_b32 v64, v84, v104, v85
	v_fmac_f32_e32 v24, v52, v52
	v_permlane32_swap_b32_e32 v6, v5
	v_add_f32_e32 v5, v6, v5
	v_add_u32_e32 v6, 0x8000, v64
	v_permlane16_swap_b32_e32 v24, v28
	v_permlane16_swap_b32_e32 v14, v26
	ds_write2_b32 v6, v2, v5 offset1:4
	v_add_f32_e32 v2, v24, v28
	v_add_f32_e32 v5, v14, v26
	s_nop 1
	v_permlane32_swap_b32_e32 v2, v5
	v_permlane16_swap_b32_e32 v16, v30
	v_permlane16_swap_b32_e32 v4, v3
	v_add_f32_e32 v2, v2, v5
	v_add_f32_e32 v5, v16, v30
	v_add_f32_e32 v3, v4, v3
	s_nop 1
	v_permlane32_swap_b32_e32 v5, v3
	v_add_f32_e32 v3, v5, v3
	ds_write2_b32 v6, v2, v3 offset0:128 offset1:132

.Lagg_invalid:
	s_or_b64 exec, exec, s[0:1]
	s_waitcnt vmcnt(0)
	ds_write_b128 v98, v[64:67]
	ds_write_b128 v98, v[68:71] offset:4096
	ds_write_b128 v98, v[72:75] offset:8192
	ds_write_b128 v98, v[76:79] offset:12288
	ds_write_b128 v98, v[80:83] offset:16384
	ds_write_b128 v98, v[84:87] offset:20480
	ds_write_b128 v98, v[88:91] offset:24576
	ds_write_b128 v98, v[92:95] offset:28672
	s_waitcnt lgkmcnt(0)
	s_barrier
	s_branch .LBB2_8

.LBB4_2:
	s_or_b64 exec, exec, s[20:21]
	v_lshlrev_b32_e32 v18, 4, v0
	s_waitcnt lgkmcnt(0)
	global_load_dwordx4 v[52:55], v18, s[4:5]
	v_add_u32_e32 v19, 0x2000, v18
	global_load_dwordx4 v[56:59], v19, s[4:5]
	v_add_u32_e32 v19, 0x4000, v18
	global_load_dwordx4 v[64:67], v19, s[4:5]
	v_add_u32_e32 v19, 0x6000, v18
	global_load_dwordx4 v[68:71], v19, s[4:5]
	v_mov_b32_e32 v72, v18
	v_lshlrev_b32_e32 v18, 2, v0
	v_or_b32_e32 v1, 0x8000, v18
	v_mov_b32_e32 v19, 0
	s_mov_b64 s[0:1], -1
	ds_write2st64_b32 v18, v19, v19 offset0:128 offset1:136
	s_and_saveexec_b64 s[4:5], s[0:1]
	ds_write_b32 v1, v19 offset:4096
	s_or_b64 exec, exec, s[4:5]
	s_and_saveexec_b64 s[4:5], s[0:1]
	v_mov_b32_e32 v19, 0
	ds_write_b32 v1, v19 offset:6144
	s_or_b64 exec, exec, s[4:5]
	s_movk_i32 s0, 0x80
	v_cmp_gt_u32_e64 s[0:1], s0, v0
	s_and_saveexec_b64 s[4:5], s[0:1]
	s_cbranch_execz .LBB4_10
	v_lshlrev_b32_e32 v20, 2, v0
	global_load_dword v19, v20, s[14:15]
	global_load_dword v26, v20, s[14:15] offset:512
	global_load_dword v27, v20, s[14:15] offset:1024
	global_load_dword v28, v20, s[14:15] offset:1536
	global_load_dword v30, v20, s[14:15] offset:2048
	global_load_dword v32, v20, s[14:15] offset:2560
	global_load_dword v34, v20, s[14:15] offset:3072
	global_load_dword v36, v20, s[14:15] offset:3584
	v_mov_b32_e32 v21, 0
	v_lshl_add_u64 v[24:25], s[14:15], 0, v[20:21]
	s_movk_i32 s0, 0x1000
	v_add_co_u32_e64 v24, s[0:1], s0, v24
	s_mov_b32 s3, 0x800000
	s_nop 0
	v_addc_co_u32_e64 v25, s[0:1], 0, v25, s[0:1]
	global_load_dword v38, v[24:25], off
	global_load_dword v39, v[24:25], off offset:512
	global_load_dword v40, v[24:25], off offset:1024
	global_load_dword v41, v[24:25], off offset:1536
	global_load_dword v42, v[24:25], off offset:2048
	global_load_dword v44, v[24:25], off offset:2560
	global_load_dword v46, v[24:25], off offset:3072
	global_load_dword v48, v[24:25], off offset:3584
	global_load_dword v50, v20, s[16:17]
	global_load_dword v51, v20, s[18:19]
	s_mov_b32 s0, 0x88e368f1
	s_mov_b32 s1, 0x3ee4f8b5
	s_waitcnt vmcnt(17)
	v_cvt_f64_f32_e32 v[20:21], v19
	s_waitcnt vmcnt(16)
	v_cvt_f64_f32_e32 v[24:25], v26
	s_waitcnt vmcnt(15)
	v_cvt_f64_f32_e32 v[26:27], v27
	v_add_f64 v[20:21], v[20:21], 0
	s_waitcnt vmcnt(13)
	v_cvt_f64_f32_e32 v[30:31], v30
	v_add_f64 v[20:21], v[20:21], v[26:27]
	v_cvt_f64_f32_e32 v[28:29], v28
	s_waitcnt vmcnt(11)
	v_cvt_f64_f32_e32 v[34:35], v34
	v_add_f64 v[24:25], v[24:25], 0
	v_add_f64 v[20:21], v[20:21], v[30:31]
	v_cvt_f64_f32_e32 v[32:33], v32
	v_add_f64 v[24:25], v[24:25], v[28:29]
	s_waitcnt vmcnt(9)
	v_cvt_f64_f32_e32 v[26:27], v38
	v_add_f64 v[20:21], v[20:21], v[34:35]
	v_cvt_f64_f32_e32 v[36:37], v36
	s_waitcnt vmcnt(8)
	v_cvt_f64_f32_e32 v[28:29], v39
	s_waitcnt vmcnt(7)
	v_cvt_f64_f32_e32 v[38:39], v40
	v_add_f64 v[24:25], v[24:25], v[32:33]
	v_add_f64 v[20:21], v[20:21], v[26:27]
	s_waitcnt vmcnt(5)
	v_cvt_f64_f32_e32 v[42:43], v42
	v_add_f64 v[24:25], v[24:25], v[36:37]
	v_add_f64 v[20:21], v[20:21], v[38:39]
	v_cvt_f64_f32_e32 v[40:41], v41
	s_waitcnt vmcnt(3)
	v_cvt_f64_f32_e32 v[46:47], v46
	v_add_f64 v[24:25], v[24:25], v[28:29]
	v_add_f64 v[20:21], v[20:21], v[42:43]
	v_cvt_f64_f32_e32 v[44:45], v44
	v_add_f64 v[24:25], v[24:25], v[40:41]
	v_add_f64 v[20:21], v[20:21], v[46:47]
	s_waitcnt vmcnt(2)
	v_cvt_f64_f32_e32 v[48:49], v48
	v_add_f64 v[24:25], v[24:25], v[44:45]
	v_mul_f64 v[20:21], v[20:21], s[0:1]
	v_add_f64 v[24:25], v[24:25], v[48:49]
	v_mul_f64 v[26:27], v[20:21], v[20:21]
	v_fma_f64 v[24:25], v[24:25], s[0:1], -v[26:27]
	v_max_f64 v[24:25], v[24:25], 0
	v_cvt_f32_f64_e32 v19, v[24:25]
	v_add_f32_e32 v19, 0x3727c5ac, v19
	v_mul_f32_e32 v24, 0x4b800000, v19
	v_cmp_gt_f32_e64 s[0:1], s3, v19
	v_cvt_f32_f64_e32 v20, v[20:21]
	s_nop 0
	v_cndmask_b32_e64 v19, v19, v24, s[0:1]
	v_rsq_f32_e32 v19, v19
	s_nop 0
	v_mul_f32_e32 v24, 0x45800000, v19
	v_cndmask_b32_e64 v19, v19, v24, s[0:1]
	s_waitcnt vmcnt(1)
	v_mul_f32_e32 v19, v50, v19
	s_waitcnt vmcnt(0)
	v_fma_f32 v20, -v19, v20, v51
	ds_write2st64_b32 v18, v19, v20 offset0:160 offset1:162
.LBB4_10:
	s_or_b64 exec, exec, s[4:5]
	s_waitcnt vmcnt(0)
	ds_write_b128 v72, v[52:55]
	ds_write_b128 v72, v[56:59] offset:8192
	ds_write_b128 v72, v[64:67] offset:16384
	ds_write_b128 v72, v[68:71] offset:24576
	s_waitcnt lgkmcnt(0)
	s_barrier
	s_and_saveexec_b64 s[0:1], vcc
	s_cbranch_execz .LBB4_12
	v_lshlrev_b32_e32 v19, 5, v23
	ds_read_b128 v[24:27], v19 offset:40960
	ds_read_b128 v[28:31], v19 offset:40976
	ds_read_b128 v[32:35], v19 offset:41472
	v_lshrrev_b32_e32 v64, 4, v22
	v_and_or_b32 v18, v18, 60, v64
	v_lshlrev_b32_e32 v18, 2, v18
	v_lshlrev_b32_e32 v65, 4, v22
	s_waitcnt lgkmcnt(0)
	v_fma_mix_f32 v20, v24, v14, v32 op_sel_hi:[0,1,0]
	v_fma_mix_f32 v14, v25, v14, v33 op_sel:[0,1,0] op_sel_hi:[0,1,0]
	v_fma_mix_f32 v21, v26, v15, v34 op_sel_hi:[0,1,0]
	v_fma_mix_f32 v15, v27, v15, v35 op_sel:[0,1,0] op_sel_hi:[0,1,0]
	ds_read_b128 v[24:27], v19 offset:41488
	v_max_f32_e32 v20, 0, v20
	v_max_f32_e32 v14, 0, v14
	v_max_f32_e32 v21, 0, v21
	v_max_f32_e32 v15, 0, v15
	s_waitcnt lgkmcnt(0)
	v_fma_mix_f32 v23, v28, v16, v24 op_sel_hi:[0,1,0]
	v_fma_mix_f32 v24, v30, v17, v26 op_sel_hi:[0,1,0]
	v_fma_mix_f32 v17, v31, v17, v27 op_sel:[0,1,0] op_sel_hi:[0,1,0]
	v_max_f32_e32 v24, 0, v24
	v_max_f32_e32 v17, 0, v17
	v_fma_mix_f32 v16, v29, v16, v25 op_sel:[0,1,0] op_sel_hi:[0,1,0]
	v_cvt_pk_f16_f32 v17, v24, v17
	ds_read_b128 v[24:27], v19 offset:41088
	ds_read_b128 v[28:31], v19 offset:41600
	v_cvt_pk_f16_f32 v15, v21, v15
	v_cvt_pk_f16_f32 v14, v20, v14
	v_max_f32_e32 v23, 0, v23
	v_max_f32_e32 v16, 0, v16
	s_waitcnt lgkmcnt(0)
	v_fma_mix_f32 v20, v24, v6, v28 op_sel_hi:[0,1,0]
	v_fma_mix_f32 v6, v25, v6, v29 op_sel:[0,1,0] op_sel_hi:[0,1,0]
	v_fma_mix_f32 v21, v26, v7, v30 op_sel_hi:[0,1,0]
	v_fma_mix_f32 v7, v27, v7, v31 op_sel:[0,1,0] op_sel_hi:[0,1,0]
	ds_read_b128 v[24:27], v19 offset:41104
	ds_read_b128 v[28:31], v19 offset:41616
	v_cvt_pk_f16_f32 v16, v23, v16
	v_max_f32_e32 v20, 0, v20
	v_max_f32_e32 v6, 0, v6
	v_max_f32_e32 v21, 0, v21
	s_waitcnt lgkmcnt(0)
	v_fma_mix_f32 v23, v24, v8, v28 op_sel_hi:[0,1,0]
	v_fma_mix_f32 v24, v26, v9, v30 op_sel_hi:[0,1,0]
	v_fma_mix_f32 v9, v27, v9, v31 op_sel:[0,1,0] op_sel_hi:[0,1,0]
	v_max_f32_e32 v24, 0, v24
	v_max_f32_e32 v9, 0, v9
	v_fma_mix_f32 v8, v25, v8, v29 op_sel:[0,1,0] op_sel_hi:[0,1,0]
	v_cvt_pk_f16_f32 v9, v24, v9
	ds_read_b128 v[24:27], v19 offset:41216
	ds_read_b128 v[28:31], v19 offset:41728
	v_max_f32_e32 v7, 0, v7
	v_cvt_pk_f16_f32 v7, v21, v7
	v_cvt_pk_f16_f32 v6, v20, v6
	v_max_f32_e32 v23, 0, v23
	s_waitcnt lgkmcnt(0)
	v_fma_mix_f32 v20, v24, v10, v28 op_sel_hi:[0,1,0]
	v_fma_mix_f32 v10, v25, v10, v29 op_sel:[0,1,0] op_sel_hi:[0,1,0]
	v_fma_mix_f32 v21, v26, v11, v30 op_sel_hi:[0,1,0]
	v_fma_mix_f32 v11, v27, v11, v31 op_sel:[0,1,0] op_sel_hi:[0,1,0]
	ds_read_b128 v[24:27], v19 offset:41232
	ds_read_b128 v[28:31], v19 offset:41744
	v_max_f32_e32 v8, 0, v8
	v_cvt_pk_f16_f32 v8, v23, v8
	v_max_f32_e32 v20, 0, v20
	v_max_f32_e32 v10, 0, v10
	s_waitcnt lgkmcnt(0)
	v_fma_mix_f32 v23, v24, v12, v28 op_sel_hi:[0,1,0]
	v_fma_mix_f32 v24, v26, v13, v30 op_sel_hi:[0,1,0]
	v_fma_mix_f32 v13, v27, v13, v31 op_sel:[0,1,0] op_sel_hi:[0,1,0]
	v_max_f32_e32 v24, 0, v24
	v_max_f32_e32 v13, 0, v13
	v_fma_mix_f32 v12, v25, v12, v29 op_sel:[0,1,0] op_sel_hi:[0,1,0]
	v_cvt_pk_f16_f32 v13, v24, v13
	ds_read_b128 v[24:27], v19 offset:41344
	ds_read_b128 v[28:31], v19 offset:41856
	v_max_f32_e32 v21, 0, v21
	v_max_f32_e32 v11, 0, v11
	v_cvt_pk_f16_f32 v11, v21, v11
	v_cvt_pk_f16_f32 v10, v20, v10
	s_waitcnt lgkmcnt(0)
	v_fma_mix_f32 v20, v24, v2, v28 op_sel_hi:[0,1,0]
	v_fma_mix_f32 v2, v25, v2, v29 op_sel:[0,1,0] op_sel_hi:[0,1,0]
	v_fma_mix_f32 v21, v26, v3, v30 op_sel_hi:[0,1,0]
	v_fma_mix_f32 v3, v27, v3, v31 op_sel:[0,1,0] op_sel_hi:[0,1,0]
	ds_read_b128 v[24:27], v19 offset:41360
	ds_read_b128 v[28:31], v19 offset:41872
	ds_bpermute_b32 v14, v18, v14
	ds_bpermute_b32 v15, v18, v15
	ds_bpermute_b32 v16, v18, v16
	ds_bpermute_b32 v17, v18, v17
	v_max_f32_e32 v23, 0, v23
	v_max_f32_e32 v12, 0, v12
	v_cvt_pk_f16_f32 v12, v23, v12
	s_waitcnt lgkmcnt(4)
	v_fma_mix_f32 v19, v24, v4, v28 op_sel_hi:[0,1,0]
	v_fma_mix_f32 v4, v25, v4, v29 op_sel:[0,1,0] op_sel_hi:[0,1,0]
	v_fma_mix_f32 v23, v26, v5, v30 op_sel_hi:[0,1,0]
	v_fma_mix_f32 v5, v27, v5, v31 op_sel:[0,1,0] op_sel_hi:[0,1,0]
	v_max_f32_e32 v20, 0, v20
	v_max_f32_e32 v2, 0, v2
	v_max_f32_e32 v21, 0, v21
	v_max_f32_e32 v3, 0, v3
	v_max_f32_e32 v19, 0, v19
	v_max_f32_e32 v4, 0, v4
	v_max_f32_e32 v23, 0, v23
	v_max_f32_e32 v5, 0, v5
	v_cvt_pk_f16_f32 v5, v23, v5
	v_cvt_pk_f16_f32 v4, v19, v4
	v_cvt_pk_f16_f32 v3, v21, v3
	v_cvt_pk_f16_f32 v2, v20, v2
	ds_bpermute_b32 v6, v18, v6
	ds_bpermute_b32 v7, v18, v7
	ds_bpermute_b32 v8, v18, v8
	ds_bpermute_b32 v9, v18, v9
	ds_bpermute_b32 v10, v18, v10
	ds_bpermute_b32 v11, v18, v11
	ds_bpermute_b32 v12, v18, v12
	ds_bpermute_b32 v13, v18, v13
	ds_bpermute_b32 v2, v18, v2
	ds_bpermute_b32 v3, v18, v3
	ds_bpermute_b32 v4, v18, v4
	ds_bpermute_b32 v5, v18, v5
	ds_read_b128 v[18:21], v65
	ds_read_b128 v[22:25], v65 offset:4096
	ds_read_b128 v[26:29], v65 offset:8192
	ds_read_b128 v[42:45], v65 offset:12288
	s_waitcnt lgkmcnt(3)
	v_mfma_f32_16x16x32_f16 v[30:33], v[14:17], v[18:21], 0
	s_waitcnt lgkmcnt(2)
	v_mfma_f32_16x16x32_f16 v[34:37], v[14:17], v[22:25], 0
	ds_read_b128 v[18:21], v65 offset:16384
	ds_read_b128 v[22:25], v65 offset:20480
	ds_read_b128 v[46:49], v65 offset:24576
	ds_read_b128 v[50:53], v65 offset:28672
	s_waitcnt lgkmcnt(5)
	v_mfma_f32_16x16x32_f16 v[38:41], v[14:17], v[26:29], 0
	s_waitcnt lgkmcnt(4)
	v_mfma_f32_16x16x32_f16 v[42:45], v[14:17], v[42:45], 0
	s_waitcnt lgkmcnt(3)
	v_mfma_f32_16x16x32_f16 v[26:29], v[14:17], v[18:21], 0
	s_waitcnt lgkmcnt(2)
	v_mfma_f32_16x16x32_f16 v[22:25], v[14:17], v[22:25], 0
	s_waitcnt lgkmcnt(1)
	v_mfma_f32_16x16x32_f16 v[18:21], v[14:17], v[46:49], 0
	s_waitcnt lgkmcnt(0)
	v_mfma_f32_16x16x32_f16 v[14:17], v[14:17], v[50:53], 0
	ds_read_b128 v[46:49], v65 offset:1024
	ds_read_b128 v[50:53], v65 offset:5120
	ds_read_b128 v[54:57], v65 offset:9216
	ds_read_b128 v[58:61], v65 offset:13312
	s_waitcnt lgkmcnt(3)
	v_mfma_f32_16x16x32_f16 v[30:33], v[6:9], v[46:49], v[30:33]
	s_waitcnt lgkmcnt(2)
	v_mfma_f32_16x16x32_f16 v[34:37], v[6:9], v[50:53], v[34:37]
	s_waitcnt lgkmcnt(1)
	v_mfma_f32_16x16x32_f16 v[38:41], v[6:9], v[54:57], v[38:41]
	s_waitcnt lgkmcnt(0)
	v_mfma_f32_16x16x32_f16 v[42:45], v[6:9], v[58:61], v[42:45]
	ds_read_b128 v[58:61], v65 offset:17408
	ds_read_b128 v[54:57], v65 offset:21504
	ds_read_b128 v[50:53], v65 offset:25600
	ds_read_b128 v[46:49], v65 offset:29696
	s_waitcnt lgkmcnt(3)
	v_mfma_f32_16x16x32_f16 v[26:29], v[6:9], v[58:61], v[26:29]
	s_waitcnt lgkmcnt(2)
	v_mfma_f32_16x16x32_f16 v[22:25], v[6:9], v[54:57], v[22:25]
	s_waitcnt lgkmcnt(1)
	v_mfma_f32_16x16x32_f16 v[18:21], v[6:9], v[50:53], v[18:21]
	s_waitcnt lgkmcnt(0)
	v_mfma_f32_16x16x32_f16 v[14:17], v[6:9], v[46:49], v[14:17]
	ds_read_b128 v[6:9], v65 offset:2048
	ds_read_b128 v[46:49], v65 offset:6144
	ds_read_b128 v[50:53], v65 offset:10240
	ds_read_b128 v[54:57], v65 offset:14336
	s_waitcnt lgkmcnt(3)
	v_mfma_f32_16x16x32_f16 v[30:33], v[10:13], v[6:9], v[30:33]
	s_waitcnt lgkmcnt(2)
	v_mfma_f32_16x16x32_f16 v[46:49], v[10:13], v[46:49], v[34:37]
	s_waitcnt lgkmcnt(1)
	v_mfma_f32_16x16x32_f16 v[50:53], v[10:13], v[50:53], v[38:41]
	s_waitcnt lgkmcnt(0)
	v_mfma_f32_16x16x32_f16 v[42:45], v[10:13], v[54:57], v[42:45]
	ds_read_b128 v[6:9], v65 offset:18432
	ds_read_b128 v[34:37], v65 offset:22528
	ds_read_b128 v[38:41], v65 offset:26624
	ds_read_b128 v[54:57], v65 offset:30720
	s_waitcnt lgkmcnt(3)
	v_mfma_f32_16x16x32_f16 v[6:9], v[10:13], v[6:9], v[26:29]
	s_waitcnt lgkmcnt(2)
	v_mfma_f32_16x16x32_f16 v[26:29], v[10:13], v[34:37], v[22:25]
	s_waitcnt lgkmcnt(1)
	v_mfma_f32_16x16x32_f16 v[34:37], v[10:13], v[38:41], v[18:21]
	s_waitcnt lgkmcnt(0)
	v_mfma_f32_16x16x32_f16 v[38:41], v[10:13], v[54:57], v[14:17]
	ds_read_b128 v[10:13], v65 offset:3072
	s_nop 1
	ds_read_b128 v[14:17], v65 offset:7168
	ds_read_b128 v[54:57], v65 offset:11264
	ds_read_b128 v[58:61], v65 offset:15360
	s_waitcnt lgkmcnt(3)
	v_mfma_f32_16x16x32_f16 v[22:25], v[2:5], v[10:13], v[30:33]
	s_waitcnt lgkmcnt(2)
	v_mfma_f32_16x16x32_f16 v[18:21], v[2:5], v[14:17], v[46:49]
	s_waitcnt lgkmcnt(1)
	v_mfma_f32_16x16x32_f16 v[14:17], v[2:5], v[54:57], v[50:53]
	s_waitcnt lgkmcnt(0)
	v_mfma_f32_16x16x32_f16 v[10:13], v[2:5], v[58:61], v[42:45]
	ds_read_b128 v[30:33], v65 offset:19456
	s_nop 1
	ds_read_b128 v[42:45], v65 offset:23552
	ds_read_b128 v[46:49], v65 offset:27648
	ds_read_b128 v[50:53], v65 offset:31744
	v_lshlrev_b32_e32 v59, 2, v64
	v_lshlrev_b32_e32 v58, 10, v62
	s_waitcnt lgkmcnt(3)
	v_mfma_f32_16x16x32_f16 v[30:33], v[2:5], v[30:33], v[6:9]
	s_waitcnt lgkmcnt(1)
	v_mfma_f32_16x16x32_f16 v[6:9], v[2:5], v[46:49], v[34:37]
	s_nop 2
	v_lshlrev_b32_e32 v34, 3, v0
	v_mfma_f32_16x16x32_f16 v[26:29], v[2:5], v[42:45], v[26:29]
	v_and_b32_e32 v44, 0x78, v34
	v_lshlrev_b32_e32 v34, 4, v63
	v_ashrrev_i32_e32 v35, 31, v34
	v_lshl_add_u64 v[36:37], v[34:35], 2, s[8:9]
	v_and_b32_e32 v42, 48, v0
	v_mov_b32_e32 v43, 0
	v_lshl_add_u64 v[36:37], v[36:37], 0, v[42:43]
	v_lshlrev_b32_e32 v42, 1, v44
	v_lshlrev_b32_e32 v60, 2, v44
	s_waitcnt lgkmcnt(0)
	v_mfma_f32_16x16x32_f16 v[2:5], v[2:5], v[50:53], v[38:41]
	v_or_b32_e32 v48, v34, v59
	v_lshl_add_u64 v[46:47], s[12:13], 0, v[42:43]
	v_mov_b32_e32 v52, v14
	global_load_dwordx4 v[38:41], v[36:37], off
	s_nop 0
	global_load_dwordx4 v[34:37], v60, s[6:7] offset:16
	global_load_dwordx4 v[42:45], v60, s[6:7]
	v_mov_b32_e32 v53, v10
	v_mov_b32_e32 v50, v22
	v_mov_b32_e32 v51, v18
	v_ashrrev_i32_e32 v49, 31, v48
	v_mov_b32_e32 v18, v23
	v_mov_b32_e32 v10, v15
	v_lshlrev_b64 v[66:67], 8, v[48:49]
	v_lshl_add_u64 v[66:67], v[46:47], 0, v[66:67]
	s_waitcnt vmcnt(0)
	v_pk_add_f32 v[52:53], v[44:45], v[52:53]
	s_nop 0
	v_pk_mul_f32 v[54:55], v[38:39], v[52:53] op_sel_hi:[0,1]
	v_mov_b32_e32 v52, v30
	v_mov_b32_e32 v53, v26
	v_pk_add_f32 v[52:53], v[34:35], v[52:53]
	v_pk_add_f32 v[50:51], v[42:43], v[50:51]
	v_pk_mul_f32 v[56:57], v[38:39], v[52:53] op_sel_hi:[0,1]
	v_mov_b32_e32 v52, v6
	v_mov_b32_e32 v53, v2
	v_pk_add_f32 v[52:53], v[36:37], v[52:53]
	v_mov_b32_e32 v26, v31
	v_mov_b32_e32 v2, v7
	v_or_b32_e32 v6, 1, v48
	v_pk_mul_f32 v[50:51], v[38:39], v[50:51] op_sel_hi:[0,1]
	v_pk_mul_f32 v[52:53], v[38:39], v[52:53] op_sel_hi:[0,1]
	v_pk_add_f32 v[18:19], v[42:43], v[18:19]
	v_pk_add_f32 v[10:11], v[44:45], v[10:11]
	v_pk_add_f32 v[14:15], v[34:35], v[26:27]
	v_pk_add_f32 v[2:3], v[36:37], v[2:3]
	v_ashrrev_i32_e32 v7, 31, v6
	v_cvt_pk_f16_f32 v62, v50, v51
	v_cvt_pk_f16_f32 v63, v54, v55
	v_cvt_pk_f16_f32 v64, v56, v57
	v_cvt_pk_f16_f32 v65, v52, v53
	v_pk_mul_f32 v[18:19], v[38:39], v[18:19] op_sel:[1,0]
	v_pk_mul_f32 v[10:11], v[38:39], v[10:11] op_sel:[1,0]
	v_pk_mul_f32 v[22:23], v[38:39], v[14:15] op_sel:[1,0]
	v_pk_mul_f32 v[2:3], v[38:39], v[2:3] op_sel:[1,0]
	v_lshlrev_b64 v[6:7], 8, v[6:7]
	global_store_dwordx4 v[66:67], v[62:65], off
	v_lshl_add_u64 v[6:7], v[46:47], 0, v[6:7]
	s_nop 0
	v_cvt_pk_f16_f32 v62, v18, v19
	v_cvt_pk_f16_f32 v63, v10, v11
	v_cvt_pk_f16_f32 v64, v22, v23
	v_cvt_pk_f16_f32 v65, v2, v3
	global_store_dwordx4 v[6:7], v[62:65], off
	v_mov_b32_e32 v6, v24
	v_mov_b32_e32 v7, v20
	v_pk_add_f32 v[6:7], v[42:43], v[6:7]
	v_mov_b32_e32 v20, v25
	v_pk_mul_f32 v[14:15], v[40:41], v[6:7] op_sel_hi:[0,1]
	v_mov_b32_e32 v6, v16
	v_mov_b32_e32 v7, v12
	v_pk_add_f32 v[6:7], v[44:45], v[6:7]
	v_mov_b32_e32 v12, v17
	v_pk_mul_f32 v[30:31], v[40:41], v[6:7] op_sel_hi:[0,1]
	v_mov_b32_e32 v6, v32
	v_mov_b32_e32 v7, v28
	v_pk_add_f32 v[6:7], v[34:35], v[6:7]
	v_mov_b32_e32 v16, v41
	v_pk_mul_f32 v[38:39], v[40:41], v[6:7] op_sel_hi:[0,1]
	v_mov_b32_e32 v6, v8
	v_mov_b32_e32 v7, v4
	v_pk_add_f32 v[6:7], v[36:37], v[6:7]
	v_pk_add_f32 v[12:13], v[44:45], v[12:13]
	v_pk_mul_f32 v[26:27], v[40:41], v[6:7] op_sel_hi:[0,1]
	v_or_b32_e32 v6, 2, v48
	v_ashrrev_i32_e32 v7, 31, v6
	v_lshlrev_b64 v[6:7], 8, v[6:7]
	v_mov_b32_e32 v28, v33
	v_cvt_pk_f16_f32 v62, v14, v15
	v_cvt_pk_f16_f32 v63, v30, v31
	v_cvt_pk_f16_f32 v64, v38, v39
	v_cvt_pk_f16_f32 v65, v26, v27
	v_lshl_add_u64 v[6:7], v[46:47], 0, v[6:7]
	v_pk_mul_f32 v[24:25], v[16:17], v[12:13] op_sel_hi:[0,1]
	v_pk_add_f32 v[12:13], v[34:35], v[28:29]
	v_add_f32_e32 v4, 0, v52
	global_store_dwordx4 v[6:7], v[62:65], off
	v_pk_add_f32 v[6:7], v[42:43], v[20:21]
	v_pk_mul_f32 v[28:29], v[16:17], v[12:13] op_sel_hi:[0,1]
	v_pk_mul_f32 v[12:13], v[2:3], v[2:3]
	v_add_f32_e32 v2, v2, v4
	v_pk_mul_f32 v[20:21], v[16:17], v[6:7] op_sel_hi:[0,1]
	v_add_f32_e32 v17, v26, v2
	v_add_f32_e32 v2, 0, v57
	v_add_f32_e32 v2, v23, v2
	v_pk_fma_f32 v[12:13], v[52:53], v[52:53], v[12:13]
	v_add_f32_e32 v2, v39, v2
	v_pk_fma_f32 v[32:33], v[26:27], v[26:27], v[12:13]
	v_pk_mul_f32 v[12:13], v[22:23], v[22:23]
	v_add_f32_e32 v26, v29, v2
	v_add_f32_e32 v2, 0, v56
	v_pk_fma_f32 v[12:13], v[56:57], v[56:57], v[12:13]
	v_add_f32_e32 v2, v22, v2
	v_pk_fma_f32 v[12:13], v[38:39], v[38:39], v[12:13]
	v_add_f32_e32 v2, v38, v2
	v_cvt_pk_f16_f32 v8, v28, v29
	v_pk_fma_f32 v[12:13], v[28:29], v[28:29], v[12:13]
	v_add_f32_e32 v28, v28, v2
	v_pk_mul_f32 v[22:23], v[10:11], v[10:11]
	v_add_f32_e32 v2, 0, v55
	v_pk_fma_f32 v[22:23], v[54:55], v[54:55], v[22:23]
	v_add_f32_e32 v2, v11, v2
	v_pk_fma_f32 v[22:23], v[30:31], v[30:31], v[22:23]
	v_add_f32_e32 v2, v31, v2
	v_cvt_pk_f16_f32 v7, v24, v25
	v_pk_fma_f32 v[22:23], v[24:25], v[24:25], v[22:23]
	v_add_f32_e32 v25, v25, v2
	v_add_f32_e32 v2, 0, v54
	v_add_f32_e32 v2, v10, v2
	v_add_f32_e32 v2, v30, v2
	v_add_f32_e32 v24, v24, v2
	v_add_f32_e32 v2, 0, v51
	v_pk_mul_f32 v[10:11], v[18:19], v[18:19]
	v_add_f32_e32 v2, v19, v2
	v_pk_fma_f32 v[10:11], v[50:51], v[50:51], v[10:11]
	v_add_f32_e32 v2, v15, v2
	v_pk_fma_f32 v[10:11], v[14:15], v[14:15], v[10:11]
	v_add_f32_e32 v15, v21, v2
	v_add_f32_e32 v2, 0, v50
	v_add_f32_e32 v2, v18, v2
	v_add_f32_e32 v2, v14, v2
	v_add_f32_e32 v14, v20, v2
	v_add_f32_e32 v2, 0, v53
	v_add_f32_e32 v2, v3, v2
	v_mov_b32_e32 v4, v9
	v_add_f32_e32 v18, v27, v2
	v_pk_add_f32 v[2:3], v[36:37], v[4:5]
	v_cvt_pk_f16_f32 v6, v20, v21
	v_pk_mul_f32 v[2:3], v[16:17], v[2:3] op_sel_hi:[0,1]
	v_cvt_pk_f16_f32 v9, v2, v3
	v_pk_fma_f32 v[4:5], v[2:3], v[2:3], v[32:33]
	v_add_f32_e32 v16, v2, v17
	v_or_b32_e32 v2, 3, v48
	v_add_f32_e32 v17, v3, v18
	v_ashrrev_i32_e32 v3, 31, v2
	v_lshlrev_b64 v[2:3], 8, v[2:3]
	v_lshl_add_u64 v[2:3], v[46:47], 0, v[2:3]
	v_permlane16_swap_b32_e32 v14, v15
	v_permlane16_swap_b32_e32 v24, v25
	global_store_dwordx4 v[2:3], v[6:9], off
	v_add_f32_e32 v2, v14, v15
	v_add_f32_e32 v3, v24, v25
	v_permlane16_swap_b32_e32 v28, v26
	v_permlane16_swap_b32_e32 v16, v17
	v_permlane32_swap_b32_e32 v2, v3
	v_add_f32_e32 v6, v28, v26
	v_add_f32_e32 v7, v16, v17
	v_add_f32_e32 v2, v2, v3
	v_or3_b32 v3, v58, v60, v59
	v_permlane32_swap_b32_e32 v6, v7
	v_pk_fma_f32 v[10:11], v[20:21], v[20:21], v[10:11]
	v_add_f32_e32 v6, v6, v7
	v_add_u32_e32 v3, 0x8000, v3
	ds_write2_b32 v3, v2, v6 offset1:4
	v_mov_b32_e32 v2, v11
	v_mov_b32_e32 v6, v23
	s_nop 0
	v_permlane16_swap_b32_e32 v10, v2
	v_permlane16_swap_b32_e32 v22, v6
	v_add_f32_e32 v2, v10, v2
	v_add_f32_e32 v6, v22, v6
	s_nop 1
	v_permlane32_swap_b32_e32 v2, v6
	v_add_f32_e32 v2, v2, v6
	v_mov_b32_e32 v6, v13
	s_nop 1
	v_permlane16_swap_b32_e32 v12, v6
	v_permlane16_swap_b32_e32 v4, v5
	v_add_f32_e32 v6, v12, v6
	v_add_f32_e32 v4, v4, v5
	s_nop 1
	v_permlane32_swap_b32_e32 v6, v4
	v_add_f32_e32 v4, v6, v4
	ds_write2_b32 v3, v2, v4 offset0:128 offset1:132

.LBB4_14:
	s_endpgm
	.p2align	8

	.amdhsa_kernel _Z6k_mlp2ILi0EEvPDF16_PKfS2_S2_PKDv8_DF16_S2_S2_Pf
		.amdhsa_group_segment_fixed_size 41984
		.amdhsa_private_segment_fixed_size 0
		.amdhsa_kernarg_size 320
		.amdhsa_user_sgpr_count 2
		.amdhsa_user_sgpr_dispatch_ptr 0
		.amdhsa_user_sgpr_queue_ptr 0
		.amdhsa_user_sgpr_kernarg_segment_ptr 1
		.amdhsa_user_sgpr_dispatch_id 0
		.amdhsa_user_sgpr_kernarg_preload_length 0
		.amdhsa_user_sgpr_kernarg_preload_offset 0
		.amdhsa_user_sgpr_private_segment_size 0
		.amdhsa_uses_dynamic_stack 0
		.amdhsa_enable_private_segment 0
		.amdhsa_system_sgpr_workgroup_id_x 1
		.amdhsa_system_sgpr_workgroup_id_y 0
		.amdhsa_system_sgpr_workgroup_id_z 0
		.amdhsa_system_sgpr_workgroup_info 0
		.amdhsa_system_vgpr_workitem_id 0
		.amdhsa_next_free_vgpr 76
		.amdhsa_next_free_sgpr 91
		.amdhsa_accum_offset 76
		.amdhsa_reserve_vcc 1
		.amdhsa_float_round_mode_32 0
		.amdhsa_float_round_mode_16_64 0
		.amdhsa_float_denorm_mode_32 3
		.amdhsa_float_denorm_mode_16_64 3
		.amdhsa_dx10_clamp 1
		.amdhsa_ieee_mode 1
		.amdhsa_fp16_overflow 0
		.amdhsa_tg_split 0
		.amdhsa_exception_fp_ieee_invalid_op 0
		.amdhsa_exception_fp_denorm_src 0
		.amdhsa_exception_fp_ieee_div_zero 0
		.amdhsa_exception_fp_ieee_overflow 0
		.amdhsa_exception_fp_ieee_underflow 0
		.amdhsa_exception_fp_ieee_inexact 0
		.amdhsa_exception_int_div_zero 0
	.end_amdhsa_kernel

	.text
	.p2alignl 8, 3212836864
	.fill 256, 4, 3212836864

amdhsa.kernels:
  - .agpr_count:     0
    .args:
      - .actual_access:  read_only
        .address_space:  global
        .offset:         0
        .size:           8
        .value_kind:     global_buffer
      - .actual_access:  read_only
        .address_space:  global
        .offset:         8
        .size:           8
        .value_kind:     global_buffer
      - .actual_access:  write_only
        .address_space:  global
        .offset:         16
        .size:           8
        .value_kind:     global_buffer
      - .actual_access:  write_only
        .address_space:  global
        .offset:         24
        .size:           8
        .value_kind:     global_buffer
      - .actual_access:  read_only
        .address_space:  global
        .offset:         32
        .size:           8
        .value_kind:     global_buffer
      - .actual_access:  read_only
        .address_space:  global
        .offset:         40
        .size:           8
        .value_kind:     global_buffer
      - .actual_access:  read_only
        .address_space:  global
        .offset:         48
        .size:           8
        .value_kind:     global_buffer
      - .actual_access:  read_only
        .address_space:  global
        .offset:         56
        .size:           8
        .value_kind:     global_buffer
      - .actual_access:  read_only
        .address_space:  global
        .offset:         64
        .size:           8
        .value_kind:     global_buffer
      - .actual_access:  read_only
        .address_space:  global
        .offset:         72
        .size:           8
        .value_kind:     global_buffer
      - .actual_access:  read_only
        .address_space:  global
        .offset:         80
        .size:           8
        .value_kind:     global_buffer
      - .actual_access:  write_only
        .address_space:  global
        .offset:         88
        .size:           8
        .value_kind:     global_buffer
      - .actual_access:  write_only
        .address_space:  global
        .offset:         96
        .size:           8
        .value_kind:     global_buffer
      - .actual_access:  write_only
        .address_space:  global
        .offset:         104
        .size:           8
        .value_kind:     global_buffer
      - .offset:         112
        .size:           4
        .value_kind:     by_value
      - .actual_access:  write_only
        .address_space:  global
        .offset:         120
        .size:           8
        .value_kind:     global_buffer
      - .offset:         128
        .size:           4
        .value_kind:     by_value
    .group_segment_fixed_size: 38944
    .kernarg_segment_align: 8
    .kernarg_segment_size: 132
    .language:       OpenCL C
    .language_version:
      - 2
      - 0
    .max_flat_workgroup_size: 512
    .name:           _Z6k_pre1PK15HIP_vector_typeIiLj4EES2_PiPjPKfS6_S6_S6_S6_S6_S6_PDF16_S7_S3_iS3_i
    .private_segment_fixed_size: 0
    .sgpr_count:     28
    .sgpr_spill_count: 0
    .symbol:         _Z6k_pre1PK15HIP_vector_typeIiLj4EES2_PiPjPKfS6_S6_S6_S6_S6_S6_PDF16_S7_S3_iS3_i.kd
    .uniform_work_group_size: 1
    .uses_dynamic_stack: false
    .vgpr_count:     61
    .vgpr_spill_count: 0
    .wavefront_size: 64
  - .agpr_count:     0
    .args:
      - .actual_access:  read_only
        .address_space:  global
        .offset:         0
        .size:           8
        .value_kind:     global_buffer
      - .actual_access:  read_only
        .address_space:  global
        .offset:         8
        .size:           8
        .value_kind:     global_buffer
      - .actual_access:  write_only
        .address_space:  global
        .offset:         16
        .size:           8
        .value_kind:     global_buffer
      - .actual_access:  write_only
        .address_space:  global
        .offset:         24
        .size:           8
        .value_kind:     global_buffer
      - .actual_access:  read_only
        .address_space:  global
        .offset:         32
        .size:           8
        .value_kind:     global_buffer
      - .actual_access:  read_only
        .address_space:  global
        .offset:         40
        .size:           8
        .value_kind:     global_buffer
      - .actual_access:  read_only
        .address_space:  global
        .offset:         48
        .size:           8
        .value_kind:     global_buffer
      - .actual_access:  read_only
        .address_space:  global
        .offset:         56
        .size:           8
        .value_kind:     global_buffer
      - .actual_access:  read_only
        .address_space:  global
        .offset:         64
        .size:           8
        .value_kind:     global_buffer
      - .actual_access:  write_only
        .address_space:  global
        .offset:         72
        .size:           8
        .value_kind:     global_buffer
      - .actual_access:  write_only
        .address_space:  global
        .offset:         80
        .size:           8
        .value_kind:     global_buffer
      - .actual_access:  write_only
        .address_space:  global
        .offset:         88
        .size:           8
        .value_kind:     global_buffer
      - .offset:         96
        .size:           4
        .value_kind:     hidden_block_count_x
      - .offset:         100
        .size:           4
        .value_kind:     hidden_block_count_y
      - .offset:         104
        .size:           4
        .value_kind:     hidden_block_count_z
      - .offset:         108
        .size:           2
        .value_kind:     hidden_group_size_x
      - .offset:         110
        .size:           2
        .value_kind:     hidden_group_size_y
      - .offset:         112
        .size:           2
        .value_kind:     hidden_group_size_z
      - .offset:         114
        .size:           2
        .value_kind:     hidden_remainder_x
      - .offset:         116
        .size:           2
        .value_kind:     hidden_remainder_y
      - .offset:         118
        .size:           2
        .value_kind:     hidden_remainder_z
      - .offset:         136
        .size:           8
        .value_kind:     hidden_global_offset_x
      - .offset:         144
        .size:           8
        .value_kind:     hidden_global_offset_y
      - .offset:         152
        .size:           8
        .value_kind:     hidden_global_offset_z
      - .offset:         160
        .size:           2
        .value_kind:     hidden_grid_dims
    .group_segment_fixed_size: 63520
    .kernarg_segment_align: 8
    .kernarg_segment_size: 352
    .language:       OpenCL C
    .language_version:
      - 2
      - 0
    .max_flat_workgroup_size: 512
    .name:           _Z6k_pre2PKjPKiPiS3_PKfPKDv8_DF16_S5_S8_S2_PDF16_PhPf
    .private_segment_fixed_size: 0
    .sgpr_count:     36
    .sgpr_spill_count: 0
    .symbol:         _Z6k_pre2PKjPKiPiS3_PKfPKDv8_DF16_S5_S8_S2_PDF16_PhPf.kd
    .uniform_work_group_size: 1
    .uses_dynamic_stack: false
    .vgpr_count:     107
    .vgpr_spill_count: 0
    .wavefront_size: 64
  - .agpr_count:     0
    .args:
      - .actual_access:  read_only
        .address_space:  global
        .offset:         0
        .size:           8
        .value_kind:     global_buffer
      - .actual_access:  read_only
        .address_space:  global
        .offset:         8
        .size:           8
        .value_kind:     global_buffer
      - .actual_access:  read_only
        .address_space:  global
        .offset:         16
        .size:           8
        .value_kind:     global_buffer
      - .actual_access:  read_only
        .address_space:  global
        .offset:         24
        .size:           8
        .value_kind:     global_buffer
      - .actual_access:  read_only
        .address_space:  global
        .offset:         32
        .size:           8
        .value_kind:     global_buffer
      - .actual_access:  read_only
        .address_space:  global
        .offset:         40
        .size:           8
        .value_kind:     global_buffer
      - .actual_access:  write_only
        .address_space:  global
        .offset:         48
        .size:           8
        .value_kind:     global_buffer
      - .address_space:  global
        .offset:         56
        .size:           8
        .value_kind:     global_buffer
      - .offset:         64
        .size:           4
        .value_kind:     hidden_block_count_x
      - .offset:         68
        .size:           4
        .value_kind:     hidden_block_count_y
      - .offset:         72
        .size:           4
        .value_kind:     hidden_block_count_z
      - .offset:         76
        .size:           2
        .value_kind:     hidden_group_size_x
      - .offset:         78
        .size:           2
        .value_kind:     hidden_group_size_y
      - .offset:         80
        .size:           2
        .value_kind:     hidden_group_size_z
      - .offset:         82
        .size:           2
        .value_kind:     hidden_remainder_x
      - .offset:         84
        .size:           2
        .value_kind:     hidden_remainder_y
      - .offset:         86
        .size:           2
        .value_kind:     hidden_remainder_z
      - .offset:         104
        .size:           8
        .value_kind:     hidden_global_offset_x
      - .offset:         112
        .size:           8
        .value_kind:     hidden_global_offset_y
      - .offset:         120
        .size:           8
        .value_kind:     hidden_global_offset_z
      - .offset:         128
        .size:           2
        .value_kind:     hidden_grid_dims
    .group_segment_fixed_size: 36864
    .kernarg_segment_align: 8
    .kernarg_segment_size: 320
    .language:       OpenCL C
    .language_version:
      - 2
      - 0
    .max_flat_workgroup_size: 256
    .name:           _Z5k_aggPKDF16_PKhPKiS4_PKDv8_DF16_PKfPDF16_Pf
    .private_segment_fixed_size: 0
    .sgpr_count:     25
    .sgpr_spill_count: 0
    .symbol:         _Z5k_aggPKDF16_PKhPKiS4_PKDv8_DF16_PKfPDF16_Pf.kd
    .uniform_work_group_size: 1
    .uses_dynamic_stack: false
    .vgpr_count:     105
    .vgpr_spill_count: 0
    .wavefront_size: 64
  - .agpr_count:     0
    .args:
      - .actual_access:  read_only
        .address_space:  global
        .offset:         0
        .size:           8
        .value_kind:     global_buffer
      - .actual_access:  read_only
        .address_space:  global
        .offset:         8
        .size:           8
        .value_kind:     global_buffer
      - .actual_access:  write_only
        .address_space:  global
        .offset:         16
        .size:           8
        .value_kind:     global_buffer
      - .offset:         24
        .size:           4
        .value_kind:     hidden_block_count_x
      - .offset:         28
        .size:           4
        .value_kind:     hidden_block_count_y
      - .offset:         32
        .size:           4
        .value_kind:     hidden_block_count_z
      - .offset:         36
        .size:           2
        .value_kind:     hidden_group_size_x
      - .offset:         38
        .size:           2
        .value_kind:     hidden_group_size_y
      - .offset:         40
        .size:           2
        .value_kind:     hidden_group_size_z
      - .offset:         42
        .size:           2
        .value_kind:     hidden_remainder_x
      - .offset:         44
        .size:           2
        .value_kind:     hidden_remainder_y
      - .offset:         46
        .size:           2
        .value_kind:     hidden_remainder_z
      - .offset:         64
        .size:           8
        .value_kind:     hidden_global_offset_x
      - .offset:         72
        .size:           8
        .value_kind:     hidden_global_offset_y
      - .offset:         80
        .size:           8
        .value_kind:     hidden_global_offset_z
      - .offset:         88
        .size:           2
        .value_kind:     hidden_grid_dims
    .group_segment_fixed_size: 0
    .kernarg_segment_align: 8
    .kernarg_segment_size: 280
    .language:       OpenCL C
    .language_version:
      - 2
      - 0
    .max_flat_workgroup_size: 1024
    .name:           _Z5k_outPKiPKfPf
    .private_segment_fixed_size: 0
    .sgpr_count:     14
    .sgpr_spill_count: 0
    .symbol:         _Z5k_outPKiPKfPf.kd
    .uniform_work_group_size: 1
    .uses_dynamic_stack: false
    .vgpr_count:     44
    .vgpr_spill_count: 0
    .wavefront_size: 64
  - .agpr_count:     0
    .args:
      - .address_space:  global
        .offset:         0
        .size:           8
        .value_kind:     global_buffer
      - .actual_access:  read_only
        .address_space:  global
        .offset:         8
        .size:           8
        .value_kind:     global_buffer
      - .actual_access:  read_only
        .address_space:  global
        .offset:         16
        .size:           8
        .value_kind:     global_buffer
      - .actual_access:  read_only
        .address_space:  global
        .offset:         24
        .size:           8
        .value_kind:     global_buffer
      - .actual_access:  read_only
        .address_space:  global
        .offset:         32
        .size:           8
        .value_kind:     global_buffer
      - .actual_access:  read_only
        .address_space:  global
        .offset:         40
        .size:           8
        .value_kind:     global_buffer
      - .actual_access:  read_only
        .address_space:  global
        .offset:         48
        .size:           8
        .value_kind:     global_buffer
      - .address_space:  global
        .offset:         56
        .size:           8
        .value_kind:     global_buffer
      - .offset:         64
        .size:           4
        .value_kind:     hidden_block_count_x
      - .offset:         68
        .size:           4
        .value_kind:     hidden_block_count_y
      - .offset:         72
        .size:           4
        .value_kind:     hidden_block_count_z
      - .offset:         76
        .size:           2
        .value_kind:     hidden_group_size_x
      - .offset:         78
        .size:           2
        .value_kind:     hidden_group_size_y
      - .offset:         80
        .size:           2
        .value_kind:     hidden_group_size_z
      - .offset:         82
        .size:           2
        .value_kind:     hidden_remainder_x
      - .offset:         84
        .size:           2
        .value_kind:     hidden_remainder_y
      - .offset:         86
        .size:           2
        .value_kind:     hidden_remainder_z
      - .offset:         104
        .size:           8
        .value_kind:     hidden_global_offset_x
      - .offset:         112
        .size:           8
        .value_kind:     hidden_global_offset_y
      - .offset:         120
        .size:           8
        .value_kind:     hidden_global_offset_z
      - .offset:         128
        .size:           2
        .value_kind:     hidden_grid_dims
    .group_segment_fixed_size: 41984
    .kernarg_segment_align: 8
    .kernarg_segment_size: 320
    .language:       OpenCL C
    .language_version:
      - 2
      - 0
    .max_flat_workgroup_size: 512
    .name:           _Z6k_mlp2ILi0EEvPDF16_PKfS2_S2_PKDv8_DF16_S2_S2_Pf
    .private_segment_fixed_size: 0
    .sgpr_count:     29
    .sgpr_spill_count: 0
    .symbol:         _Z6k_mlp2ILi0EEvPDF16_PKfS2_S2_PKDv8_DF16_S2_S2_Pf.kd
    .uniform_work_group_size: 1
    .uses_dynamic_stack: false
    .vgpr_count:     76
    .vgpr_spill_count: 0
    .wavefront_size: 64
  - .agpr_count:     0
    .args:
      - .actual_access:  read_only
        .address_space:  global
        .offset:         0
        .size:           8
        .value_kind:     global_buffer
      - .actual_access:  read_only
        .address_space:  global
        .offset:         8
        .size:           8
        .value_kind:     global_buffer
      - .actual_access:  read_only
        .address_space:  global
        .offset:         16
        .size:           8
        .value_kind:     global_buffer
      - .actual_access:  read_only
        .address_space:  global
        .offset:         24
        .size:           8
        .value_kind:     global_buffer
      - .address_space:  global
        .offset:         32
        .size:           8
        .value_kind:     global_buffer
      - .actual_access:  write_only
        .address_space:  global
        .offset:         40
        .size:           8
        .value_kind:     global_buffer
      - .actual_access:  read_only
        .address_space:  global
        .offset:         48
        .size:           8
        .value_kind:     global_buffer
      - .actual_access:  read_only
        .address_space:  global
        .offset:         56
        .size:           8
        .value_kind:     global_buffer
      - .actual_access:  read_only
        .address_space:  global
        .offset:         64
        .size:           8
        .value_kind:     global_buffer
      - .address_space:  global
        .offset:         72
        .size:           8
        .value_kind:     global_buffer
    .group_segment_fixed_size: 1024
    .kernarg_segment_align: 8
    .kernarg_segment_size: 80
    .language:       OpenCL C
    .language_version:
      - 2
      - 0
    .max_flat_workgroup_size: 512
    .name:           _Z8k_updateILi1EEvPKDF16_PKfS3_S3_PDF16_PhPKDv8_DF16_PKiPfSB_
    .private_segment_fixed_size: 0
    .sgpr_count:     25
    .sgpr_spill_count: 0
    .symbol:         _Z8k_updateILi1EEvPKDF16_PKfS3_S3_PDF16_PhPKDv8_DF16_PKiPfSB_.kd
    .uniform_work_group_size: 1
    .uses_dynamic_stack: false
    .vgpr_count:     112
    .vgpr_spill_count: 0
    .wavefront_size: 64
  - .agpr_count:     0
    .args:
      - .actual_access:  read_only
        .address_space:  global
        .offset:         0
        .size:           8
        .value_kind:     global_buffer
      - .actual_access:  read_only
        .address_space:  global
        .offset:         8
        .size:           8
        .value_kind:     global_buffer
      - .actual_access:  read_only
        .address_space:  global
        .offset:         16
        .size:           8
        .value_kind:     global_buffer
      - .actual_access:  read_only
        .address_space:  global
        .offset:         24
        .size:           8
        .value_kind:     global_buffer
      - .actual_access:  read_only
        .address_space:  global
        .offset:         32
        .size:           8
        .value_kind:     global_buffer
      - .actual_access:  read_only
        .address_space:  global
        .offset:         40
        .size:           8
        .value_kind:     global_buffer
      - .actual_access:  read_only
        .address_space:  global
        .offset:         48
        .size:           8
        .value_kind:     global_buffer
      - .actual_access:  read_only
        .address_space:  global
        .offset:         56
        .size:           8
        .value_kind:     global_buffer
      - .address_space:  global
        .offset:         64
        .size:           8
        .value_kind:     global_buffer
      - .actual_access:  read_only
        .address_space:  global
        .offset:         72
        .size:           8
        .value_kind:     global_buffer
    .group_segment_fixed_size: 6656
    .kernarg_segment_align: 8
    .kernarg_segment_size: 80
    .language:       OpenCL C
    .language_version:
      - 2
      - 0
    .max_flat_workgroup_size: 512
    .name:           _Z8k_updateILi2EEvPKDF16_PKfS3_S3_PDF16_PhPKDv8_DF16_PKiPfSB_
    .private_segment_fixed_size: 0
    .sgpr_count:     36
    .sgpr_spill_count: 0
    .symbol:         _Z8k_updateILi2EEvPKDF16_PKfS3_S3_PDF16_PhPKDv8_DF16_PKiPfSB_.kd
    .uniform_work_group_size: 1
    .uses_dynamic_stack: false
    .vgpr_count:     104
    .vgpr_spill_count: 0
    .wavefront_size: 64
